# v55 stack + combine phase prefetches all 8 residual rows of the wave at phase entry
# baseline (speedup 1.0000x reference)
; #define GAS __attribute__((address_space(1)))
; #define LAS __attribute__((address_space(3)))
; __device__ __forceinline__ void phase_combine(Frame& F, int l) {
;     const int gw = F.vcu * NWAVES + F.wave, NGW = F.G * NWAVES, lane = F.lane;
;     const GAS float* modl = (const GAS float*)(F.ws + WS_MOD) + (size_t)l * 4 * 6144;
;     const GAS int* slot = (const GAS int*)(F.ws + WS_SLOT); const GAS bf16* ye = (const GAS bf16*)(F.ws + WS_YE);
;     LAS float* PV = (LAS float*)F.lds;
;     for (int i = F.tid; i < 4 * 256; i += NTHR) { const int b = i >> 8, c4 = i & 255; const GAS float* mb = modl + (size_t)b * 6144;
;         const f32x4 gf = ((const GAS f32x4*)(mb + 5120))[c4], pg = ((const GAS f32x4*)(INP(F, I_FPOST) + l * DM))[c4];
;         LAS f32x4* pv = (LAS f32x4*)(PV + b * 3072) + ((c4 >> 2) + 64 * (c4 & 3)); pv[0] = gf * pg;
;         if (l + 1 < DEPTH) { const GAS float* mn = modl + 4 * 6144 + (size_t)b * 6144; const f32x4 gg = ((const GAS f32x4*)(INP(F, I_MPRE) + (l + 1) * DM))[c4], s1 = ((const GAS f32x4*)(mn + 1024))[c4], s0 = ((const GAS f32x4*)mn)[c4];
;             pv[256] = gg * (1.0f + s1); pv[512] = s0; } }
;     __syncthreads();
;     for (int m0 = gw; m0 < M; m0 += 2 * NGW) {
;         int mm[2]; mm[0] = m0; mm[1] = (m0 + NGW < M) ? m0 + NGW : m0;
;         int sl[2]; unsigned long long mask[2]; f32x4 y[2][4], x[2][4];
; #pragma unroll
;         for (int q = 0; q < 2; ++q) { const int b = mm[q] >> 12, t = mm[q] & (SEQ - 1); sl[q] = -1; if (lane < 16) sl[q] = slot[((size_t)b * NEXP + lane) * SEQ + t];
;             roww_load_bf16((const GAS bf16*)(F.ws + WS_XR) + (size_t)mm[q] * DM, lane, x[q]);
.LBB0_1947:
	s_cmp_le_i32 s86, s38
	s_cselect_b64 s[0:1], -1, 0
	s_and_b64 s[0:1], s[0:1], s[34:35]
	v_cndmask_b32_e64 v1, 0, 1, s[0:1]
	v_cmp_ne_u32_e64 s[4:5], 1, v1
	s_mov_b64 s[58:59], s[80:81]
	s_andn2_b64 vcc, exec, s[0:1]
	s_cbranch_vccnz .LBB0_1955
	v_lshrrev_b32_e32 v250, 6, v0
	v_and_b32_e32 v248, 63, v0
	s_and_b32 s20, s88, 7
	s_lshl_b32 s20, s20, 5
	s_lshr_b32 s21, s88, 3
	s_add_u32 s20, s20, s21
	s_lshl_b32 s20, s20, 3
	v_readfirstlane_b32 s21, v250
	v_lshrrev_b32_e32 v249, 5, v248
	v_and_b32_e32 v248, 31, v248
	s_add_u32 s20, s20, s21
	v_lshlrev_b32_e32 v248, 6, v248
	s_lshl_b32 s21, s20, 11
	v_lshl_add_u32 v248, v249, 22, v248
	s_add_u32 s22, s58, 0x27400000
	s_addc_u32 s23, s59, 0
	s_add_u32 s22, s22, s21
	s_addc_u32 s23, s23, 0
	global_load_dword v253, v248, s[22:23]
	s_add_u32 s22, s22, 0x800000
	s_addc_u32 s23, s23, 0
	global_load_dword v253, v248, s[22:23]
	s_add_u32 s22, s22, 0x800000
	s_addc_u32 s23, s23, 0
	global_load_dword v253, v248, s[22:23]
	s_add_u32 s22, s22, 0x800000
	s_addc_u32 s23, s23, 0
	global_load_dword v253, v248, s[22:23]
	v_readlane_b32 s0, v254, 8
	v_readlane_b32 s1, v254, 9
	v_readlane_b32 s30, v255, 3
	v_writelane_b32 v254, s0, 8
	v_readlane_b32 s31, v255, 4
	s_nop 0
	v_writelane_b32 v254, s1, 9
	s_nop 0
	v_readlane_b32 s12, v254, 2
	s_and_b32 s0, s12, 7
	s_cmp_lg_u32 s0, 0
	v_readlane_b32 s13, v254, 30
	v_readlane_b32 s19, v254, 47
	v_readlane_b32 s20, v254, 48
	s_cbranch_scc1 .LBB0_1950
	s_lshr_b32 s0, s12, 3
	v_readlane_b32 s1, v254, 22
	s_mul_i32 s0, s0, s1
	v_readlane_b32 s1, v254, 26
	s_add_i32 s0, s0, s1
	s_lshl_b32 s13, s0, 3
